# barriers in front of Fourier stage C and of the final phase arrive-only too: completion awaited after the constant-matrix loads / after the final phase's gain, gate and slot loads
# speedup vs baseline: 1.0088x; 1.0030x over previous
.LBB0_456:
	s_or_b64 exec, exec, s[10:11]
	v_cvt_f32_u32_e32 v4, v2
	s_waitcnt vmcnt(1)
	v_readfirstlane_b32 s8, v3
	v_sub_u32_e32 v3, 0, v2
	v_rcp_iflag_f32_e32 v4, v4
	v_add_u32_e32 v5, s8, v1
	v_mul_f32_e32 v4, 0x4f7ffffe, v4
	v_cvt_u32_f32_e32 v4, v4
	v_mul_lo_u32 v1, v3, v4
	v_mul_hi_u32 v1, v4, v1
	v_add_u32_e32 v1, v4, v1
	v_mul_hi_u32 v1, v5, v1
	v_mul_lo_u32 v3, v1, v2
	v_sub_u32_e32 v3, v5, v3
	v_add_u32_e32 v4, 1, v1
	v_cmp_ge_u32_e32 vcc, v3, v2
	s_nop 1
	v_cndmask_b32_e32 v1, v1, v4, vcc
	v_sub_u32_e32 v4, v3, v2
	v_cndmask_b32_e32 v3, v3, v4, vcc
	v_add_u32_e32 v4, 1, v1
	v_cmp_ge_u32_e32 vcc, v3, v2
	v_add_u32_e32 v3, 1, v5
	s_nop 0
	v_cndmask_b32_e32 v1, v1, v4, vcc
	v_mul_lo_u32 v4, v2, v1
	v_add_u32_e32 v2, v4, v2
	v_readlane_b32 s100, v235, 7
	v_readlane_b32 s101, v235, 8
	v_add_u32_e32 v236, 1, v1
	s_waitcnt lgkmcnt(0)
	v_mul_lo_u32 v236, v236, v0
	v_mov_b32_e32 v237, 0x3400
	v_mov_b32_e32 v239, 0
	v_cmp_ne_u32_e32 vcc, v3, v2
	s_cbranch_vccnz .Lxb_poll_4
	buffer_wbl2 sc1
	s_waitcnt vmcnt(0)
	v_mov_b32_e32 v238, 1
	global_atomic_add v237, v238, s[100:101]
.Lxb_poll_4:
	v_readfirstlane_b32 s98, v236
	s_branch .Lxb_done_4

.LBB0_491:
	s_or_b64 exec, exec, s[0:1]
	v_readlane_b32 s0, v235, 16
	v_readlane_b32 s1, v235, 17
	s_lshl_b32 s8, s0, 4
	v_readlane_b32 s0, v235, 0
	v_readlane_b32 s1, v235, 1
	s_mov_b64 s[14:15], s[46:47]
	s_waitcnt lgkmcnt(0)
	v_mov_b32_e32 v0, v186
	s_barrier
	s_load_dwordx2 s[0:1], s[14:15], 0x98
	s_waitcnt vmcnt(14)
	v_ashrrev_i32_e32 v68, 5, v0
	v_readlane_b32 s2, v235, 2
	v_and_b32_e32 v1, -2, v68
	s_lshl_b32 s20, s2, 4
	v_add_u32_e32 v70, s8, v1
	s_movk_i32 s2, 0x2000
	v_readlane_b32 s3, v235, 3
	v_cmp_gt_i32_e32 vcc, s2, v70
	v_writelane_b32 v235, s8, 18
	s_and_saveexec_b64 s[2:3], vcc
	s_cbranch_execz .LBB0_494
	v_bfe_u32 v69, v0, 4, 2
	v_and_b32_e32 v71, 15, v0
	v_lshlrev_b32_e32 v64, 4, v69
	v_mov_b32_e32 v65, 0
	v_lshlrev_b32_e32 v0, 8, v71
	v_mov_b32_e32 v1, v65
	s_waitcnt lgkmcnt(0)
	v_lshl_add_u64 v[66:67], s[0:1], 0, v[64:65]
	v_lshl_add_u64 v[48:49], v[66:67], 0, v[0:1]
	v_add_co_u32_e32 v18, vcc, 0x1adb000, v48
	s_mov_b64 s[8:9], 0x1adb000
	s_nop 0
	v_addc_co_u32_e32 v19, vcc, 0, v49, vcc
	v_add_co_u32_e32 v32, vcc, 0x1adc000, v48
	v_lshl_add_u64 v[16:17], v[48:49], 0, s[8:9]
	s_nop 0
	v_addc_co_u32_e32 v33, vcc, 0, v49, vcc
	v_add_co_u32_e32 v50, vcc, 0x1add000, v48
	global_load_dwordx4 v[0:3], v[16:17], off offset:64
	global_load_dwordx4 v[4:7], v[16:17], off offset:128
	global_load_dwordx4 v[8:11], v[18:19], off
	global_load_dwordx4 v[12:15], v[16:17], off offset:192
	v_addc_co_u32_e32 v51, vcc, 0, v49, vcc
	s_waitcnt vmcnt(17)
	v_add_co_u32_e32 v72, vcc, 0x1ade000, v48
	global_load_dwordx4 v[16:19], v[32:33], off
	global_load_dwordx4 v[20:23], v[32:33], off offset:64
	global_load_dwordx4 v[24:27], v[32:33], off offset:128
	global_load_dwordx4 v[28:31], v[32:33], off offset:192
	v_addc_co_u32_e32 v73, vcc, 0, v49, vcc
	global_load_dwordx4 v[32:35], v[50:51], off
	global_load_dwordx4 v[36:39], v[50:51], off offset:64
	global_load_dwordx4 v[40:43], v[50:51], off offset:128
	global_load_dwordx4 v[44:47], v[50:51], off offset:192
	s_nop 0
	global_load_dwordx4 v[48:51], v[72:73], off
	global_load_dwordx4 v[52:55], v[72:73], off offset:64
	global_load_dwordx4 v[56:59], v[72:73], off offset:128
	global_load_dwordx4 v[60:63], v[72:73], off offset:192
	s_mov_b64 s[10:11], 0x132f3000
	v_lshl_add_u64 v[66:67], v[66:67], 0, s[10:11]
	v_lshrrev_b32_e32 v64, 1, v68
	v_readlane_b32 s10, v235, 16
	v_readlane_b32 s16, v235, 0
	s_add_u32 s8, s0, 0x1971b000
	v_lshlrev_b32_e32 v68, 2, v64
	v_readlane_b32 s11, v235, 17
	v_readlane_b32 s17, v235, 1
	v_readlane_b32 s18, v235, 2
	v_lshlrev_b32_e32 v64, 5, v64
	s_addc_u32 s9, s1, 0
	v_lshlrev_b32_e32 v72, 9, v69
	v_lshl_add_u32 v73, s10, 5, v68
	s_lshl_b32 s12, s18, 5
	v_lshl_add_u32 v74, s10, 8, v64
	s_lshl_b32 s13, s18, 8
	s_mov_b64 s[10:11], 0
	s_movk_i32 s16, 0x60
	s_movk_i32 s17, 0x1fff
	v_readlane_b32 s19, v235, 3
	v_readfirstlane_b32 s100, v186
	s_nop 0
	s_cmp_lg_u32 s100, 0
	s_cbranch_scc1 .Ldfc_w_skip
	s_cmp_eq_u32 s98, 0
	s_cbranch_scc1 .Ldfc_w_skip
	v_readlane_b32 s100, v235, 7
	v_readlane_b32 s101, v235, 8
	v_mov_b32_e32 v236, 0x3400
	v_mov_b32_e32 v239, 0
	s_nop 3

.Ldfc_w_skip:
	s_barrier
.LBB0_493:
	s_waitcnt vmcnt(25)
	v_add_u32_e32 v88, v71, v74
	s_waitcnt vmcnt(24)
	v_add_u32_e32 v92, 16, v88
	v_ashrrev_i32_e32 v89, 31, v88
	v_ashrrev_i32_e32 v93, 31, v92
	v_lshlrev_b64 v[68:69], 8, v[88:89]
	v_lshlrev_b64 v[92:93], 8, v[92:93]
	v_lshl_add_u64 v[68:69], v[66:67], 0, v[68:69]
	v_lshl_add_u64 v[120:121], v[66:67], 0, v[92:93]
	global_load_dwordx4 v[76:79], v[68:69], off
	global_load_dwordx4 v[80:83], v[68:69], off offset:64
	global_load_dwordx4 v[96:99], v[120:121], off
	global_load_dwordx4 v[100:103], v[120:121], off offset:64
	v_bfe_u32 v75, v70, 5, 7
	v_and_b32_e32 v112, 0xffffe000, v73
	v_or3_b32 v116, v75, v112, v72
	v_and_b32_e32 v64, 0x180, v74
	v_and_or_b32 v117, v74, s16, v71
	v_lshlrev_b32_e32 v64, 1, v64
	v_lshl_add_u64 v[118:119], s[8:9], 0, v[64:65]
	v_lshlrev_b32_e32 v64, 1, v117
	v_ashrrev_i32_e32 v117, 31, v116
	v_or_b32_e32 v122, 0x80, v116
	v_or_b32_e32 v124, 0x100, v116
	v_or_b32_e32 v126, 0x180, v116
	v_or_b32_e32 v128, 0x800, v116
	v_or_b32_e32 v130, 0x880, v116
	v_or_b32_e32 v132, 0x900, v116
	v_or_b32_e32 v134, 0x980, v116
	v_or_b32_e32 v136, 0x1000, v116
	v_or_b32_e32 v138, 0x1080, v116
	v_or_b32_e32 v140, 0x1100, v116
	v_or_b32_e32 v142, 0x1180, v116
	v_or_b32_e32 v144, 0x1800, v116
	v_or_b32_e32 v146, 0x1880, v116
	v_or_b32_e32 v148, 0x1900, v116
	v_or_b32_e32 v150, 0x1980, v116
	v_lshl_add_u64 v[152:153], v[118:119], 0, v[64:65]
	v_lshlrev_b64 v[154:155], 11, v[116:117]
	v_add_u32_e32 v70, s20, v70
	v_ashrrev_i32_e32 v123, 31, v122
	v_ashrrev_i32_e32 v125, 31, v124
	v_ashrrev_i32_e32 v127, 31, v126
	v_ashrrev_i32_e32 v129, 31, v128
	v_ashrrev_i32_e32 v131, 31, v130
	v_ashrrev_i32_e32 v133, 31, v132
	v_ashrrev_i32_e32 v135, 31, v134
	v_ashrrev_i32_e32 v137, 31, v136
	v_ashrrev_i32_e32 v139, 31, v138
	v_ashrrev_i32_e32 v141, 31, v140
	v_ashrrev_i32_e32 v143, 31, v142
	v_ashrrev_i32_e32 v145, 31, v144
	v_ashrrev_i32_e32 v147, 31, v146
	v_ashrrev_i32_e32 v149, 31, v148
	v_ashrrev_i32_e32 v151, 31, v150
	v_cmp_lt_i32_e32 vcc, s17, v70
	v_add_u32_e32 v73, s12, v73
	v_add_u32_e32 v74, s13, v74
	s_or_b64 s[10:11], vcc, s[10:11]
	s_waitcnt vmcnt(3)
	v_mfma_f32_16x16x32_bf16 v[84:87], v[8:11], v[76:79], 0
	v_mfma_f32_16x16x32_bf16 v[88:91], v[16:19], v[76:79], 0
	v_mfma_f32_16x16x32_bf16 v[92:95], v[32:35], v[76:79], 0
	v_mfma_f32_16x16x32_bf16 v[76:79], v[48:51], v[76:79], 0
	s_waitcnt vmcnt(1)
	v_mfma_f32_16x16x32_bf16 v[104:107], v[8:11], v[96:99], 0
	v_mfma_f32_16x16x32_bf16 v[108:111], v[16:19], v[96:99], 0
	v_mfma_f32_16x16x32_bf16 v[112:115], v[32:35], v[96:99], 0
	v_mfma_f32_16x16x32_bf16 v[96:99], v[48:51], v[96:99], 0
	v_mfma_f32_16x16x32_bf16 v[84:87], v[0:3], v[80:83], v[84:87]
	v_mfma_f32_16x16x32_bf16 v[88:91], v[20:23], v[80:83], v[88:91]
	v_mfma_f32_16x16x32_bf16 v[92:95], v[36:39], v[80:83], v[92:95]
	v_mfma_f32_16x16x32_bf16 v[76:79], v[52:55], v[80:83], v[76:79]
	s_waitcnt vmcnt(0)
	v_mfma_f32_16x16x32_bf16 v[80:83], v[0:3], v[100:103], v[104:107]
	v_mfma_f32_16x16x32_bf16 v[104:107], v[20:23], v[100:103], v[108:111]
	v_mfma_f32_16x16x32_bf16 v[108:111], v[36:39], v[100:103], v[112:115]
	v_mfma_f32_16x16x32_bf16 v[96:99], v[52:55], v[100:103], v[96:99]
	global_load_dwordx4 v[100:103], v[68:69], off offset:128
	s_nop 0
	global_load_dwordx4 v[112:115], v[68:69], off offset:192
	global_load_dwordx4 v[116:119], v[120:121], off offset:128
	v_lshl_add_u64 v[68:69], v[152:153], 0, v[154:155]
	s_waitcnt vmcnt(2)
	v_mfma_f32_16x16x32_bf16 v[84:87], v[4:7], v[100:103], v[84:87]
	v_mfma_f32_16x16x32_bf16 v[88:91], v[24:27], v[100:103], v[88:91]
	v_mfma_f32_16x16x32_bf16 v[92:95], v[40:43], v[100:103], v[92:95]
	v_mfma_f32_16x16x32_bf16 v[76:79], v[56:59], v[100:103], v[76:79]
	global_load_dwordx4 v[100:103], v[120:121], off offset:192
	v_lshlrev_b64 v[120:121], 11, v[122:123]
	v_lshlrev_b64 v[122:123], 11, v[124:125]
	s_waitcnt vmcnt(1)
	v_mfma_f32_16x16x32_bf16 v[80:83], v[4:7], v[116:119], v[80:83]
	v_lshlrev_b64 v[124:125], 11, v[126:127]
	v_lshlrev_b64 v[126:127], 11, v[128:129]
	v_lshlrev_b64 v[128:129], 11, v[130:131]
	v_mfma_f32_16x16x32_bf16 v[104:107], v[24:27], v[116:119], v[104:107]
	v_lshlrev_b64 v[130:131], 11, v[132:133]
	v_lshlrev_b64 v[132:133], 11, v[138:139]
	v_lshlrev_b64 v[138:139], 11, v[144:145]
	v_mfma_f32_16x16x32_bf16 v[108:111], v[40:43], v[116:119], v[108:111]
	v_lshlrev_b64 v[144:145], 11, v[150:151]
	v_lshl_add_u64 v[120:121], v[152:153], 0, v[120:121]
	v_lshl_add_u64 v[122:123], v[152:153], 0, v[122:123]
	v_mfma_f32_16x16x32_bf16 v[96:99], v[56:59], v[116:119], v[96:99]
	v_lshlrev_b64 v[116:117], 11, v[134:135]
	v_lshlrev_b64 v[118:119], 11, v[136:137]
	v_lshlrev_b64 v[134:135], 11, v[140:141]
	v_mfma_f32_16x16x32_bf16 v[84:87], v[12:15], v[112:115], v[84:87]
	v_lshlrev_b64 v[136:137], 11, v[142:143]
	v_lshlrev_b64 v[140:141], 11, v[146:147]
	v_lshlrev_b64 v[142:143], 11, v[148:149]
	v_mfma_f32_16x16x32_bf16 v[88:91], v[28:31], v[112:115], v[88:91]
	v_lshl_add_u64 v[124:125], v[152:153], 0, v[124:125]
	s_nop 2
	v_cvt_pk_bf16_f32 v64, v84, s0
	v_lshl_add_u64 v[116:117], v[152:153], 0, v[116:117]
	v_mfma_f32_16x16x32_bf16 v[92:95], v[44:47], v[112:115], v[92:95]
	v_lshl_add_u64 v[118:119], v[152:153], 0, v[118:119]
	v_cvt_pk_bf16_f32 v75, v85, s0
	v_cvt_pk_bf16_f32 v84, v86, s0
	v_mfma_f32_16x16x32_bf16 v[76:79], v[60:63], v[112:115], v[76:79]
	v_lshl_add_u64 v[112:113], v[152:153], 0, v[126:127]
	v_lshl_add_u64 v[114:115], v[152:153], 0, v[128:129]
	v_lshl_add_u64 v[126:127], v[152:153], 0, v[130:131]
	s_waitcnt vmcnt(0)
	v_mfma_f32_16x16x32_bf16 v[80:83], v[12:15], v[100:103], v[80:83]
	v_lshl_add_u64 v[128:129], v[152:153], 0, v[132:133]
	v_lshl_add_u64 v[130:131], v[152:153], 0, v[134:135]
	v_lshl_add_u64 v[132:133], v[152:153], 0, v[136:137]
	v_mfma_f32_16x16x32_bf16 v[104:107], v[28:31], v[100:103], v[104:107]
	v_lshl_add_u64 v[134:135], v[152:153], 0, v[138:139]
	v_lshl_add_u64 v[136:137], v[152:153], 0, v[140:141]
	v_lshl_add_u64 v[138:139], v[152:153], 0, v[142:143]
	v_mfma_f32_16x16x32_bf16 v[108:111], v[44:47], v[100:103], v[108:111]
	v_lshl_add_u64 v[140:141], v[152:153], 0, v[144:145]
	v_cvt_pk_bf16_f32 v85, v87, s0
	v_cvt_pk_bf16_f32 v86, v88, s0
	v_mfma_f32_16x16x32_bf16 v[96:99], v[60:63], v[100:103], v[96:99]
	v_cvt_pk_bf16_f32 v87, v89, s0
	v_cvt_pk_bf16_f32 v88, v90, s0
	v_cvt_pk_bf16_f32 v89, v91, s0
	v_cvt_pk_bf16_f32 v90, v92, s0
	v_cvt_pk_bf16_f32 v91, v93, s0
	v_cvt_pk_bf16_f32 v92, v94, s0
	v_cvt_pk_bf16_f32 v93, v95, s0
	v_cvt_pk_bf16_f32 v76, v76, s0
	v_cvt_pk_bf16_f32 v77, v77, s0
	v_cvt_pk_bf16_f32 v78, v78, s0
	v_cvt_pk_bf16_f32 v79, v79, s0
	global_store_short v[68:69], v64, off
	global_store_short v[120:121], v75, off
	global_store_short v[122:123], v84, off
	global_store_short v[124:125], v85, off
	global_store_short v[112:113], v86, off
	global_store_short v[114:115], v87, off
	global_store_short v[126:127], v88, off
	global_store_short v[116:117], v89, off
	global_store_short v[118:119], v90, off
	global_store_short v[128:129], v91, off
	global_store_short v[130:131], v92, off
	global_store_short v[132:133], v93, off
	global_store_short v[134:135], v76, off
	global_store_short v[136:137], v77, off
	global_store_short v[138:139], v78, off
	global_store_short v[140:141], v79, off
	v_cvt_pk_bf16_f32 v64, v80, s0
	v_cvt_pk_bf16_f32 v75, v81, s0
	v_cvt_pk_bf16_f32 v76, v82, s0
	v_cvt_pk_bf16_f32 v77, v83, s0
	v_cvt_pk_bf16_f32 v78, v104, s0
	v_cvt_pk_bf16_f32 v79, v105, s0
	v_cvt_pk_bf16_f32 v80, v106, s0
	v_cvt_pk_bf16_f32 v81, v107, s0
	v_cvt_pk_bf16_f32 v82, v108, s0
	v_cvt_pk_bf16_f32 v83, v109, s0
	v_cvt_pk_bf16_f32 v84, v110, s0
	v_cvt_pk_bf16_f32 v85, v111, s0
	v_cvt_pk_bf16_f32 v86, v96, s0
	v_cvt_pk_bf16_f32 v87, v97, s0
	v_cvt_pk_bf16_f32 v88, v98, s0
	v_cvt_pk_bf16_f32 v89, v99, s0
	global_store_short v[68:69], v64, off offset:32
	global_store_short v[120:121], v75, off offset:32
	global_store_short v[122:123], v76, off offset:32
	global_store_short v[124:125], v77, off offset:32
	global_store_short v[112:113], v78, off offset:32
	global_store_short v[114:115], v79, off offset:32
	global_store_short v[126:127], v80, off offset:32
	global_store_short v[116:117], v81, off offset:32
	global_store_short v[118:119], v82, off offset:32
	global_store_short v[128:129], v83, off offset:32
	global_store_short v[130:131], v84, off offset:32
	global_store_short v[132:133], v85, off offset:32
	global_store_short v[134:135], v86, off offset:32
	global_store_short v[136:137], v87, off offset:32
	global_store_short v[138:139], v88, off offset:32
	global_store_short v[140:141], v89, off offset:32
	s_andn2_b64 exec, exec, s[10:11]
	s_cbranch_execnz .LBB0_493

.LBB0_1241:
	s_or_b64 exec, exec, s[0:1]
	s_waitcnt lgkmcnt(0)
	s_barrier
	v_readlane_b32 s6, v235, 16
	v_readlane_b32 s7, v235, 2
	v_and_b32_e32 v0, 63, v186
	v_lshrrev_b32_e32 v11, 6, v186
	s_load_dwordx2 s[4:5], s[46:47], 0x98
	s_load_dwordx4 s[0:3], s[46:47], 0x88
	v_readfirstlane_b32 s8, v11
	v_lshlrev_b32_e32 v1, 4, v0
	v_lshlrev_b32_e32 v11, 14, v11
	v_add_u32_e32 v11, v11, v1
	v_lshlrev_b32_e32 v2, 5, v0
	v_and_b32_e32 v3, 31, v0
	v_lshlrev_b32_e32 v3, 2, v3
	v_xor_b32_e32 v4, 32, v0
	v_lshlrev_b32_e32 v4, 2, v4
	v_xor_b32_e32 v5, 16, v0
	v_lshlrev_b32_e32 v5, 2, v5
	v_xor_b32_e32 v6, 8, v0
	v_lshlrev_b32_e32 v6, 2, v6
	v_xor_b32_e32 v7, 4, v0
	v_lshlrev_b32_e32 v7, 2, v7
	v_xor_b32_e32 v8, 2, v0
	v_lshlrev_b32_e32 v8, 2, v8
	v_xor_b32_e32 v9, 1, v0
	v_lshlrev_b32_e32 v9, 2, v9
	v_mov_b32_e32 v10, 0x358637bd
	s_lshl_b32 s6, s6, 4
	s_lshl_b32 s8, s8, 1
	s_add_i32 s6, s6, s8
	s_lshl_b32 s7, s7, 4
	s_mov_b32 s23, 0x3a800000
	s_cmp_lt_u32 s6, 0x4000
	s_cbranch_scc0 .Lfin_end
	s_waitcnt lgkmcnt(0)
	s_add_u32 s14, s4, 0x1b73000
	s_addc_u32 s15, s5, 0
	s_add_u32 s16, s4, 0x9f73000
	s_addc_u32 s17, s5, 0
	s_add_u32 s18, s4, 0x15b000
	s_addc_u32 s19, s5, 0
	s_add_u32 s20, s4, 0x5000
	s_addc_u32 s21, s5, 0
	s_add_u32 s34, s20, 0x6000
	s_addc_u32 s35, s21, 0
	global_load_dwordx4 v[12:15], v2, s[0:1]
	global_load_dwordx4 v[16:19], v2, s[0:1] offset:16
	global_load_dwordx4 v[20:23], v2, s[0:1] offset:2048
	global_load_dwordx4 v[24:27], v2, s[0:1] offset:2064
	global_load_dwordx4 v[28:31], v2, s[20:21]
	global_load_dwordx4 v[32:35], v2, s[20:21] offset:16
	global_load_dwordx4 v[36:39], v2, s[20:21] offset:2048
	global_load_dwordx4 v[40:43], v2, s[20:21] offset:2064
	global_load_dwordx4 v[44:47], v2, s[34:35]
	global_load_dwordx4 v[48:51], v2, s[34:35] offset:16
	global_load_dwordx4 v[52:55], v2, s[34:35] offset:2048
	global_load_dwordx4 v[56:59], v2, s[34:35] offset:2064
	s_lshl_b32 s26, s6, 6
	s_add_u32 s24, s18, s26
	s_addc_u32 s25, s19, 0
	global_load_dword v77, v3, s[24:25]
	s_waitcnt vmcnt(0)
	v_readfirstlane_b32 s100, v186
	s_nop 0
	s_cmp_lg_u32 s100, 0
	s_cbranch_scc1 .Lp11_w_skip
	s_cmp_eq_u32 s98, 0
	s_cbranch_scc1 .Lp11_w_skip
	v_readlane_b32 s100, v235, 7
	v_readlane_b32 s101, v235, 8
	v_mov_b32_e32 v236, 0x3400
	v_mov_b32_e32 v239, 0
	s_nop 3

.Lp11_w_skip:
	s_barrier
	s_branch .Lfin_body
